# cmp and window QK: K ds_reads issued before the per-item scalar/VALU setup, full lgkmcnt(0) replaced by counted waits per MFMA pair
# speedup vs baseline: 1.0020x; 1.0008x over previous
; #define LAS __attribute__((address_space(3)))
; #define SBAR() __builtin_amdgcn_sched_barrier(0)
;     i32x8a kf[4];
; #pragma unroll
;     for (int T_ = 0; T_ < 4; ++T_) { kf[T_].lo = *(const LAS i32x4a*)(kl8 + T_ * 16 * K8ST); kf[T_].hi = *(const LAS i32x4a*)(kl8 + T_ * 16 * K8ST + 16); }
;     asm volatile("s_waitcnt lgkmcnt(0)" ::: "memory"); SBAR();
; #pragma unroll
;     for (int T_ = 0; T_ < 4; ++T_) { s0[T_] = __builtin_amdgcn_mfma_scale_f32_16x16x128_f8f6f4(kf[T_], g0.q8, (f32x4){c0, c0, c0, c0}, 0, 0, 0, 0x7f7f7f7f, 0, 0x7c7c7c7c);
;         s1[T_] = __builtin_amdgcn_mfma_scale_f32_16x16x128_f8f6f4(kf[T_], g1.q8, (f32x4){c1, c1, c1, c1}, 0, 0, 0, 0x7f7f7f7f, 0, 0x7c7c7c7c); }
; }
; __device__ __forceinline__ void mask_scores(f32x4 (&s)[4], int a, unsigned W, int kb, int q4) {
;     const float NEG = -__builtin_inff();
; #pragma unroll
;     for (int T_ = 0; T_ < 4; ++T_)
; #pragma unroll
;         for (int i = 0; i < 4; ++i) if ((unsigned)(a - (kb + 16 * T_ + 4 * q4 + i)) >= W) s[T_][i] = NEG;
; }
; __device__ __forceinline__ void window_phase(Frame& F) {
;     ...
;             const float r0 = smc_ref(g0), r1 = smc_ref(g1);
;             qk8_tile2(s0, s1, g0, g1, sb + klane, -r0, -r1);
;             if (j == 0 || j == nblk - 1) { mask_scores(s0, tokA, (unsigned)WIN, kb, kq); mask_scores(s1, tokA + 4, (unsigned)WIN, kb, kq); }
.LBB0_1489:
	s_and_b32 s6, s36, 3
	s_mulk_i32 s6, 0x6c00
	s_add_i32 s6, s6, 0
	v_add3_u32 v88, s6, v143, v116
	ds_read_b128 v[80:83], v88
	ds_read_b128 v[84:87], v88 offset:16
	ds_read_b128 v[158:161], v88 offset:2304
	ds_read_b128 v[162:165], v88 offset:2320
	ds_read_b128 v[166:169], v88 offset:4608
	ds_read_b128 v[170:173], v88 offset:4624
	ds_read_b128 v[174:177], v88 offset:6912
	ds_read_b128 v[178:181], v88 offset:6928
	v_cmp_ngt_f32_e32 vcc, s49, v137
	s_nop 1
	v_cndmask_b32_e32 v136, 0, v137, vcc
	v_cmp_ngt_f32_e32 vcc, s49, v135
	v_xor_b32_e32 v96, 0x80000000, v136
	s_nop 0
	v_cndmask_b32_e32 v134, 0, v135, vcc
	v_xor_b32_e32 v182, 0x80000000, v134
	v_mov_b32_e32 v97, v96
	v_mov_b32_e32 v98, v96
	v_mov_b32_e32 v99, v96
	v_mov_b32_e32 v183, v182
	v_mov_b32_e32 v184, v182
	v_mov_b32_e32 v185, v182
	s_waitcnt lgkmcnt(6)
	v_mfma_scale_f32_16x16x128_f8f6f4 v[100:103], v[80:87], v[0:7], v[96:99], v149, v148 op_sel_hi:[0,0,0]
	s_cmp_lg_u32 s52, s36
	v_mfma_scale_f32_16x16x128_f8f6f4 v[92:95], v[80:87], v[8:15], v[182:185], v149, v148 op_sel_hi:[0,0,0]
	s_waitcnt lgkmcnt(4)
	v_mfma_scale_f32_16x16x128_f8f6f4 v[108:111], v[158:165], v[0:7], v[96:99], v149, v148 op_sel_hi:[0,0,0]
	v_mfma_scale_f32_16x16x128_f8f6f4 v[88:91], v[158:165], v[8:15], v[182:185], v149, v148 op_sel_hi:[0,0,0]
	s_waitcnt lgkmcnt(2)
	v_mfma_scale_f32_16x16x128_f8f6f4 v[104:107], v[166:173], v[0:7], v[96:99], v149, v148 op_sel_hi:[0,0,0]
	v_mfma_scale_f32_16x16x128_f8f6f4 v[80:83], v[166:173], v[8:15], v[182:185], v149, v148 op_sel_hi:[0,0,0]
	s_waitcnt lgkmcnt(0)
	v_mfma_scale_f32_16x16x128_f8f6f4 v[96:99], v[174:181], v[0:7], v[96:99], v149, v148 op_sel_hi:[0,0,0]
	v_mfma_scale_f32_16x16x128_f8f6f4 v[84:87], v[174:181], v[8:15], v[182:185], v149, v148 op_sel_hi:[0,0,0]
	s_cbranch_scc1 .LBB0_1491
	v_add_u32_e32 v138, s34, v156
	v_subrev_u32_e32 v139, 64, v138
	v_mov_b32_e32 v130, s46
	v_cmp_gt_u32_e32 vcc, s45, v139
	v_add_u32_e32 v139, s34, v155
	v_add_u32_e32 v157, 0xffffffb0, v138
	v_cndmask_b32_e32 v100, v130, v100, vcc
	v_add_u32_e32 v130, 4, v154
	v_cmp_lt_u32_e32 vcc, s47, v130
	v_add_u32_e32 v130, 0xffffffbe, v139
	s_nop 0
	v_cndmask_b32_e32 v101, v150, v101, vcc
	v_cmp_gt_u32_e32 vcc, s45, v130
	v_add_u32_e32 v130, 0xffffffbd, v139
	s_nop 0
	v_cndmask_b32_e32 v102, v150, v102, vcc
	v_cmp_gt_u32_e32 vcc, s45, v130
	v_mov_b32_e32 v130, s46
	s_nop 0
	v_cndmask_b32_e32 v103, v150, v103, vcc
	v_cmp_gt_u32_e32 vcc, s45, v157
	v_add_u32_e32 v157, 0xffffffa0, v138
	v_add_u32_e32 v138, 0xffffff90, v138
	v_cndmask_b32_e32 v108, v130, v108, vcc
	v_add_u32_e32 v130, 0xffffffaf, v139
	v_cmp_gt_u32_e32 vcc, s45, v130
	v_add_u32_e32 v130, 0xffffffae, v139
	s_nop 0
	v_cndmask_b32_e32 v109, v150, v109, vcc
	v_cmp_gt_u32_e32 vcc, s45, v130
	v_add_u32_e32 v130, 0xffffffad, v139
	s_nop 0
	v_cndmask_b32_e32 v110, v150, v110, vcc
	v_cmp_gt_u32_e32 vcc, s45, v130
	v_mov_b32_e32 v130, s46
	s_nop 0
	v_cndmask_b32_e32 v111, v150, v111, vcc
	v_cmp_gt_u32_e32 vcc, s45, v157
	s_nop 1
	v_cndmask_b32_e32 v104, v130, v104, vcc
	v_add_u32_e32 v130, 0xffffff9f, v139
	v_cmp_gt_u32_e32 vcc, s45, v130
	v_add_u32_e32 v130, 0xffffff9e, v139
	s_nop 0
	v_cndmask_b32_e32 v105, v150, v105, vcc
	v_cmp_gt_u32_e32 vcc, s45, v130
	v_add_u32_e32 v130, 0xffffff9d, v139
	s_nop 0
	v_cndmask_b32_e32 v106, v150, v106, vcc
	v_cmp_gt_u32_e32 vcc, s45, v130
	v_mov_b32_e32 v130, s46
	s_nop 0
	v_cndmask_b32_e32 v107, v150, v107, vcc
	v_cmp_gt_u32_e32 vcc, s45, v138
	v_subrev_u32_e32 v138, 60, v139
	s_nop 0
	v_cndmask_b32_e32 v96, v130, v96, vcc
	v_add_u32_e32 v130, 0xffffff8f, v139
	v_cmp_gt_u32_e32 vcc, s45, v130
	v_add_u32_e32 v130, 0xffffff8e, v139
	s_nop 0
	v_cndmask_b32_e32 v97, v150, v97, vcc
	v_cmp_gt_u32_e32 vcc, s45, v130
	v_add_u32_e32 v130, 0xffffff8d, v139
	s_nop 0
	v_cndmask_b32_e32 v98, v150, v98, vcc
	v_cmp_gt_u32_e32 vcc, s45, v130
	v_mov_b32_e32 v130, s46
	s_nop 0
	v_cndmask_b32_e32 v99, v150, v99, vcc
	v_cmp_gt_u32_e32 vcc, s45, v138
	v_add_u32_e32 v138, 0xffffffb4, v139
	s_nop 0
	v_cndmask_b32_e32 v92, v130, v92, vcc
	v_cmp_lt_u32_e32 vcc, s47, v154
	v_subrev_u32_e32 v130, 62, v139
	s_nop 0
	v_cndmask_b32_e32 v93, v150, v93, vcc
	v_cmp_gt_u32_e32 vcc, s45, v130
	v_subrev_u32_e32 v130, 63, v139
	s_nop 0
	v_cndmask_b32_e32 v94, v150, v94, vcc
	v_cmp_gt_u32_e32 vcc, s45, v130
	v_mov_b32_e32 v130, s46
	s_nop 0
	v_cndmask_b32_e32 v95, v150, v95, vcc
	v_cmp_gt_u32_e32 vcc, s45, v138
	v_add_u32_e32 v138, 0xffffffa4, v139
	s_nop 0
	v_cndmask_b32_e32 v88, v130, v88, vcc
	v_add_u32_e32 v130, 0xffffffb3, v139
	v_cmp_gt_u32_e32 vcc, s45, v130
	v_add_u32_e32 v130, 0xffffffb2, v139
	s_nop 0
	v_cndmask_b32_e32 v89, v150, v89, vcc
	v_cmp_gt_u32_e32 vcc, s45, v130
	v_add_u32_e32 v130, 0xffffffb1, v139
	s_nop 0
	v_cndmask_b32_e32 v90, v150, v90, vcc
	v_cmp_gt_u32_e32 vcc, s45, v130
	v_mov_b32_e32 v130, s46
	s_nop 0
	v_cndmask_b32_e32 v91, v150, v91, vcc
	v_cmp_gt_u32_e32 vcc, s45, v138
	v_add_u32_e32 v138, 0xffffff94, v139
	s_nop 0
	v_cndmask_b32_e32 v80, v130, v80, vcc
	v_add_u32_e32 v130, 0xffffffa3, v139
	v_cmp_gt_u32_e32 vcc, s45, v130
	v_add_u32_e32 v130, 0xffffffa2, v139
	s_nop 0
	v_cndmask_b32_e32 v81, v150, v81, vcc
	v_cmp_gt_u32_e32 vcc, s45, v130
	v_add_u32_e32 v130, 0xffffffa1, v139
	s_nop 0
	v_cndmask_b32_e32 v82, v150, v82, vcc
	v_cmp_gt_u32_e32 vcc, s45, v130
	v_mov_b32_e32 v130, s46
	s_nop 0
	v_cndmask_b32_e32 v83, v150, v83, vcc
	v_cmp_gt_u32_e32 vcc, s45, v138
	s_nop 1
	v_cndmask_b32_e32 v84, v130, v84, vcc
	v_add_u32_e32 v130, 0xffffff93, v139
	v_cmp_gt_u32_e32 vcc, s45, v130
	v_add_u32_e32 v130, 0xffffff92, v139
	s_nop 0
	v_cndmask_b32_e32 v85, v150, v85, vcc
	v_cmp_gt_u32_e32 vcc, s45, v130
	v_add_u32_e32 v130, 0xffffff91, v139
	s_nop 0
	v_cndmask_b32_e32 v86, v150, v86, vcc
	v_cmp_gt_u32_e32 vcc, s45, v130
	s_nop 1
	v_cndmask_b32_e32 v87, v150, v87, vcc

; #define LAS __attribute__((address_space(3)))
; #define SBAR() __builtin_amdgcn_sched_barrier(0)
;     i32x8a kf[4];
; #pragma unroll
;     for (int T_ = 0; T_ < 4; ++T_) { kf[T_].lo = *(const LAS i32x4a*)(kl8 + T_ * 16 * K8ST); kf[T_].hi = *(const LAS i32x4a*)(kl8 + T_ * 16 * K8ST + 16); }
;     asm volatile("s_waitcnt lgkmcnt(0)" ::: "memory"); SBAR();
; #pragma unroll
;     for (int T_ = 0; T_ < 4; ++T_) { s0[T_] = __builtin_amdgcn_mfma_scale_f32_16x16x128_f8f6f4(kf[T_], g0.q8, (f32x4){c0, c0, c0, c0}, 0, 0, 0, 0x7f7f7f7f, 0, 0x7c7c7c7c);
;         s1[T_] = __builtin_amdgcn_mfma_scale_f32_16x16x128_f8f6f4(kf[T_], g1.q8, (f32x4){c1, c1, c1, c1}, 0, 0, 0, 0x7f7f7f7f, 0, 0x7c7c7c7c); }
; }
; __device__ __forceinline__ void mask_scores(f32x4 (&s)[4], int a, unsigned W, int kb, int q4) {
;     const float NEG = -__builtin_inff();
; #pragma unroll
;     for (int T_ = 0; T_ < 4; ++T_)
; #pragma unroll
;         for (int i = 0; i < 4; ++i) if ((unsigned)(a - (kb + 16 * T_ + 4 * q4 + i)) >= W) s[T_][i] = NEG;
; }
; __device__ __forceinline__ void cmp_phase(Frame& F) {
;     ...
;             const bool p1 = i < nkt; const float r0 = p1 ? smc_ref(g0) : g0.m - __builtin_amdgcn_logf(i0), r1 = p1 ? smc_ref(g1) : g1.m - __builtin_amdgcn_logf(i1);
;             f32x4 s0[4], s1[4];
;             qk8_tile2(s0, s1, g0, g1, sb + klane, -r0, -r1);
;             if (kt * 64 + 63 > ((t0 - 31) >> 4)) { mask_scores(s0, limA, 0x40000000u, kt * 64, kq); mask_scores(s1, limB, 0x40000000u, kt * 64, kq); }
.LBB0_1577:
	s_bitcmp1_b32 s80, 0
	s_cselect_b32 s22, 0x6c00, 0
	s_add_i32 s37, s22, 0
	v_add3_u32 v88, s37, v174, v118
	ds_read_b128 v[80:83], v88
	ds_read_b128 v[84:87], v88 offset:16
	ds_read_b128 v[92:95], v88 offset:2304
	ds_read_b128 v[96:99], v88 offset:2320
	ds_read_b128 v[144:147], v88 offset:4608
	ds_read_b128 v[148:151], v88 offset:4624
	ds_read_b128 v[152:155], v88 offset:6912
	ds_read_b128 v[156:159], v88 offset:6928
	s_cmp_le_u32 s80, s60
	s_cselect_b64 s[56:57], -1, 0
	v_log_f32_e32 v161, v113
	s_cmp_gt_u32 s80, s60
	v_cmp_ngt_f32_e32 vcc, s68, v141
	v_log_f32_e32 v165, v142
	v_sub_f32_e32 v161, v141, v161
	v_cndmask_b32_e32 v140, 0, v141, vcc
	s_cselect_b64 vcc, -1, 0
	s_and_b64 s[22:23], vcc, exec
	v_cmp_ngt_f32_e64 s[22:23], s68, v139
	v_sub_f32_e32 v165, v139, v165
	v_cndmask_b32_e32 v161, v140, v161, vcc
	v_cndmask_b32_e64 v138, 0, v139, s[22:23]
	v_cndmask_b32_e32 v165, v138, v165, vcc
	v_xor_b32_e32 v160, 0x80000000, v161
	v_xor_b32_e32 v164, 0x80000000, v165
	s_cselect_b32 s48, s61, 0
	v_mov_b32_e32 v161, v160
	v_mov_b32_e32 v162, v160
	v_mov_b32_e32 v163, v160
	v_mov_b32_e32 v165, v164
	v_mov_b32_e32 v166, v164
	v_mov_b32_e32 v167, v164
	s_waitcnt lgkmcnt(6)
	v_mfma_scale_f32_16x16x128_f8f6f4 v[108:111], v[80:87], v[0:7], v[160:163], v181, v180 op_sel_hi:[0,0,0]
	s_lshl_b32 s22, s48, 6
	s_sub_i32 s48, 0, s22
	s_sub_i32 s23, s79, s22
	s_cmp_le_i32 s23, s75
	v_mfma_scale_f32_16x16x128_f8f6f4 v[88:91], v[80:87], v[8:15], v[164:167], v181, v180 op_sel_hi:[0,0,0]
	s_waitcnt lgkmcnt(4)
	v_mfma_scale_f32_16x16x128_f8f6f4 v[104:107], v[92:99], v[0:7], v[160:163], v181, v180 op_sel_hi:[0,0,0]
	v_mfma_scale_f32_16x16x128_f8f6f4 v[84:87], v[92:99], v[8:15], v[164:167], v181, v180 op_sel_hi:[0,0,0]
	s_waitcnt lgkmcnt(2)
	v_mfma_scale_f32_16x16x128_f8f6f4 v[100:103], v[144:151], v[0:7], v[160:163], v181, v180 op_sel_hi:[0,0,0]
	v_mfma_scale_f32_16x16x128_f8f6f4 v[80:83], v[144:151], v[8:15], v[164:167], v181, v180 op_sel_hi:[0,0,0]
	s_waitcnt lgkmcnt(0)
	v_mfma_scale_f32_16x16x128_f8f6f4 v[96:99], v[152:159], v[0:7], v[160:163], v181, v180 op_sel_hi:[0,0,0]
	v_mfma_scale_f32_16x16x128_f8f6f4 v[92:95], v[152:159], v[8:15], v[164:167], v181, v180 op_sel_hi:[0,0,0]
	s_cbranch_scc1 .LBB0_1579
	s_add_i32 s22, s22, s59
	s_add_i32 s23, s48, s79
	v_add_u32_e32 v134, s22, v188
	v_add_u32_e32 v144, s23, v189
	v_cmp_gt_u32_e32 vcc, 2.0, v134
	v_subrev_u32_e32 v144, 63, v144
	s_nop 0
	v_cndmask_b32_e32 v108, v182, v108, vcc
	v_cmp_lt_u32_e32 vcc, s69, v144
	v_add_u32_e32 v144, -2, v134
	s_nop 0
	v_cndmask_b32_e32 v109, v182, v109, vcc
	v_cmp_gt_u32_e32 vcc, 2.0, v144
	v_add_u32_e32 v144, -3, v134
	s_nop 0
	v_cndmask_b32_e32 v110, v182, v110, vcc
	v_cmp_gt_u32_e32 vcc, 2.0, v144
	v_add_u32_e32 v144, -16, v134
	s_nop 0
	v_cndmask_b32_e32 v111, v182, v111, vcc
	v_cmp_gt_u32_e32 vcc, 2.0, v144
	v_subrev_u32_e32 v144, 17, v134
	s_nop 0
	v_cndmask_b32_e32 v104, v182, v104, vcc
	v_cmp_gt_u32_e32 vcc, 2.0, v144
	v_subrev_u32_e32 v144, 18, v134
	s_nop 0
	v_cndmask_b32_e32 v105, v182, v105, vcc
	v_cmp_gt_u32_e32 vcc, 2.0, v144
	v_subrev_u32_e32 v144, 19, v134
	s_nop 0
	v_cndmask_b32_e32 v106, v182, v106, vcc
	v_cmp_gt_u32_e32 vcc, 2.0, v144
	v_subrev_u32_e32 v144, 32, v134
	s_nop 0
	v_cndmask_b32_e32 v107, v182, v107, vcc
	v_cmp_gt_u32_e32 vcc, 2.0, v144
	v_subrev_u32_e32 v144, 33, v134
	s_nop 0
	v_cndmask_b32_e32 v100, v182, v100, vcc
	v_cmp_gt_u32_e32 vcc, 2.0, v144
	v_subrev_u32_e32 v144, 34, v134
	s_nop 0
	v_cndmask_b32_e32 v101, v182, v101, vcc
	v_cmp_gt_u32_e32 vcc, 2.0, v144
	v_subrev_u32_e32 v144, 35, v134
	s_nop 0
	v_cndmask_b32_e32 v102, v182, v102, vcc
	v_cmp_gt_u32_e32 vcc, 2.0, v144
	v_subrev_u32_e32 v144, 48, v134
	s_nop 0
	v_cndmask_b32_e32 v103, v182, v103, vcc
	v_cmp_gt_u32_e32 vcc, 2.0, v144
	v_subrev_u32_e32 v144, 49, v134
	s_nop 0
	v_cndmask_b32_e32 v96, v182, v96, vcc
	v_cmp_gt_u32_e32 vcc, 2.0, v144
	v_subrev_u32_e32 v144, 50, v134
	v_subrev_u32_e32 v134, 51, v134
	v_cndmask_b32_e32 v97, v182, v97, vcc
	v_cmp_gt_u32_e32 vcc, 2.0, v144
	v_add_u32_e32 v144, s23, v186
	v_subrev_u32_e32 v144, 63, v144
	v_cndmask_b32_e32 v98, v182, v98, vcc
	v_cmp_gt_u32_e32 vcc, 2.0, v134
	v_add_u32_e32 v134, s22, v187
	s_nop 0
	v_cndmask_b32_e32 v99, v182, v99, vcc
	v_cmp_gt_u32_e32 vcc, 2.0, v134
	s_nop 1
	v_cndmask_b32_e32 v88, v182, v88, vcc
	v_cmp_lt_u32_e32 vcc, s69, v144
	v_add_u32_e32 v144, -2, v134
	s_nop 0
	v_cndmask_b32_e32 v89, v182, v89, vcc
	v_cmp_gt_u32_e32 vcc, 2.0, v144
	v_add_u32_e32 v144, -3, v134
	s_nop 0
	v_cndmask_b32_e32 v90, v182, v90, vcc
	v_cmp_gt_u32_e32 vcc, 2.0, v144
	v_add_u32_e32 v144, -16, v134
	s_nop 0
	v_cndmask_b32_e32 v91, v182, v91, vcc
	v_cmp_gt_u32_e32 vcc, 2.0, v144
	v_subrev_u32_e32 v144, 17, v134
	s_nop 0
	v_cndmask_b32_e32 v84, v182, v84, vcc
	v_cmp_gt_u32_e32 vcc, 2.0, v144
	v_subrev_u32_e32 v144, 18, v134
	s_nop 0
	v_cndmask_b32_e32 v85, v182, v85, vcc
	v_cmp_gt_u32_e32 vcc, 2.0, v144
	v_subrev_u32_e32 v144, 19, v134
	s_nop 0
	v_cndmask_b32_e32 v86, v182, v86, vcc
	v_cmp_gt_u32_e32 vcc, 2.0, v144
	v_subrev_u32_e32 v144, 32, v134
	s_nop 0
	v_cndmask_b32_e32 v87, v182, v87, vcc
	v_cmp_gt_u32_e32 vcc, 2.0, v144
	v_subrev_u32_e32 v144, 33, v134
	s_nop 0
	v_cndmask_b32_e32 v80, v182, v80, vcc
	v_cmp_gt_u32_e32 vcc, 2.0, v144
	v_subrev_u32_e32 v144, 34, v134
	s_nop 0
	v_cndmask_b32_e32 v81, v182, v81, vcc
	v_cmp_gt_u32_e32 vcc, 2.0, v144
	v_subrev_u32_e32 v144, 35, v134
	s_nop 0
	v_cndmask_b32_e32 v82, v182, v82, vcc
	v_cmp_gt_u32_e32 vcc, 2.0, v144
	v_subrev_u32_e32 v144, 48, v134
	s_nop 0
	v_cndmask_b32_e32 v83, v182, v83, vcc
	v_cmp_gt_u32_e32 vcc, 2.0, v144
	v_subrev_u32_e32 v144, 49, v134
	s_nop 0
	v_cndmask_b32_e32 v92, v182, v92, vcc
	v_cmp_gt_u32_e32 vcc, 2.0, v144
	v_subrev_u32_e32 v144, 50, v134
	v_subrev_u32_e32 v134, 51, v134
	v_cndmask_b32_e32 v93, v182, v93, vcc
	v_cmp_gt_u32_e32 vcc, 2.0, v144
	s_nop 1
	v_cndmask_b32_e32 v94, v182, v94, vcc
	v_cmp_gt_u32_e32 vcc, 2.0, v134
	s_nop 1
	v_cndmask_b32_e32 v95, v182, v95, vcc
